# rot
# speedup vs baseline: 1.0044x; 1.0044x over previous
_Z10lstm_fusedPKfS0_S0_S0_S0_S0_S0_S0_S0_S0_S0_Pf:
	s_load_dwordx16 s[36:51], s[0:1], 0x0
	s_load_dwordx8 s[52:59], s[0:1], 0x40
	s_load_dword s21, s[0:1], 0x60
	v_readfirstlane_b32 s3, v0
	v_and_b32_e32 v69, 63, v0
	v_and_b32_e32 v68, 15, v0
	v_bfe_u32 v1, v0, 4, 2
	s_lshr_b32 s3, s3, 6
	s_add_u32 s27, s3, s2
	s_and_b32 s27, s27, 15
	s_lshl_b32 s28, s27, 10
	s_lshl_b32 s29, s27, 6
	s_lshl_b32 s2, s2, 4
	s_add_i32 s20, s3, s2
	v_lshlrev_b32_e32 v2, 5, v1
	v_mov_b32_e32 v3, 0
	v_lshl_add_u32 v60, v69, 4, s28
	s_lshl_b32 s26, s20, 12
	s_waitcnt lgkmcnt(0)
	s_load_dword s34, s[56:57], 0x0
	v_lshl_add_u64 v[42:43], s[36:37], 0, v[2:3]
	v_lshl_or_b32 v2, v68, 7, s26
	v_lshl_add_u64 v[74:75], v[42:43], 0, v[2:3]
	s_add_u32 s4, s27, 0
	s_mov_b32 s24, 0
	s_mov_b32 s25, 0
	s_sub_u32 s5, s4, 12
	s_mov_b64 s[8:9], s[44:45]
	s_movk_i32 s10, 0x100
	s_movk_i32 s11, 16
	s_movk_i32 s12, 64
	s_mov_b32 s13, 0xbf2562dd
	s_mov_b32 s14, 0xbfa562dd
	s_mov_b32 s15, 1
	s_cmp_lt_u32 s4, 12
	s_cbranch_scc0 .Lpr0_cls
	s_lshl_b32 s5, s4, 1
	s_mov_b64 s[8:9], s[38:39]
	s_movk_i32 s10, 0x80
	s_movk_i32 s11, 32
	s_movk_i32 s12, 16
	s_mov_b32 s13, 0xbfb8aa3b
	s_mov_b32 s14, 0xc038aa3b
.Lpr0_cls:
	s_lshr_b32 s6, s5, 1
	s_and_b32 s7, s5, 1
	s_lshl_b32 s7, s7, 7
	s_mul_i32 s16, s6, 43
	s_lshr_b32 s16, s16, 7
	s_mul_i32 s17, s16, 3
	s_sub_u32 s17, s6, s17
	s_min_u32 s18, s17, 1
	s_add_u32 s18, s18, s17
	s_lshl_b32 s18, s18, 6
	s_lshl_b32 s19, s16, 4
	s_add_u32 s18, s18, s19
	s_lshl_b32 s19, s6, 4
	s_cmp_eq_u32 s15, 1
	s_cselect_b32 s18, s18, s19
	s_cmp_eq_u32 s17, 1
	s_cselect_b32 s19, s14, s13
	s_cmp_eq_u32 s15, 1
	s_cselect_b32 s13, s19, s13
	s_mul_i32 s18, s18, s10
	s_add_u32 s18, s18, s7
	s_add_u32 s22, s8, s12
	s_addc_u32 s23, s9, 0
	v_mul_u32_u24_e32 v57, s10, v68
	v_mad_u32_u24 v57, v1, s11, v57
	v_add_u32_e32 v54, s18, v57
	v_mov_b32_e32 v48, s13
	global_load_dwordx4 v[18:21], v54, s[8:9]
	global_load_dwordx4 v[22:25], v54, s[22:23]
	s_add_u32 s4, s27, 16
	s_mov_b32 s24, 0
	s_mov_b32 s25, 0
	s_sub_u32 s5, s4, 12
	s_mov_b64 s[8:9], s[44:45]
	s_movk_i32 s10, 0x100
	s_movk_i32 s11, 16
	s_movk_i32 s12, 64
	s_mov_b32 s13, 0xbf2562dd
	s_mov_b32 s14, 0xbfa562dd
	s_mov_b32 s15, 1
.Lpr1_cls:
	s_lshr_b32 s6, s5, 1
	s_and_b32 s7, s5, 1
	s_lshl_b32 s7, s7, 7
	s_mul_i32 s16, s6, 43
	s_lshr_b32 s16, s16, 7
	s_mul_i32 s17, s16, 3
	s_sub_u32 s17, s6, s17
	s_min_u32 s18, s17, 1
	s_add_u32 s18, s18, s17
	s_lshl_b32 s18, s18, 6
	s_lshl_b32 s19, s16, 4
	s_add_u32 s18, s18, s19
	s_lshl_b32 s19, s6, 4
	s_cmp_eq_u32 s15, 1
	s_cselect_b32 s18, s18, s19
	s_cmp_eq_u32 s17, 1
	s_cselect_b32 s19, s14, s13
	s_cmp_eq_u32 s15, 1
	s_cselect_b32 s13, s19, s13
	s_mul_i32 s18, s18, s10
	s_add_u32 s18, s18, s7
	s_add_u32 s22, s8, s12
	s_addc_u32 s23, s9, 0
	v_mul_u32_u24_e32 v57, s10, v68
	v_mad_u32_u24 v57, v1, s11, v57
	v_add_u32_e32 v55, s18, v57
	v_mov_b32_e32 v50, s13
	global_load_dwordx4 v[26:29], v55, s[8:9]
	global_load_dwordx4 v[30:33], v55, s[22:23]
	s_add_u32 s4, s27, 32
	s_mov_b32 s24, 0
	s_mov_b32 s25, 0
	s_sub_u32 s5, s4, 12
	s_mov_b64 s[8:9], s[44:45]
	s_movk_i32 s10, 0x100
	s_movk_i32 s11, 16
	s_movk_i32 s12, 64
	s_mov_b32 s13, 0xbf2562dd
	s_mov_b32 s14, 0xbfa562dd
	s_mov_b32 s15, 1
	s_cmp_lt_u32 s4, 36
	s_cbranch_scc1 .Lpr2_cls
	s_mov_b32 s15, 0
	s_sub_u32 s5, s4, 36
	s_mov_b64 s[8:9], s[50:51]
	s_mov_b32 s13, 0x3ee54621
	s_cmp_lt_u32 s4, 40
	s_cbranch_scc1 .Lpr2_cls
	s_mov_b32 s5, 0
	s_mov_b64 s[8:9], s[54:55]
	s_movk_i32 s10, 0
	s_mov_b32 s13, 0xbfb8aa3b
	s_mov_b32 s24, 1
	s_cmp_gt_u32 s4, 40
	s_cselect_b32 s25, 1, 0

.Lpr2_nofc2:
	global_load_dwordx4 v[34:37], v56, s[8:9]
	global_load_dwordx4 v[44:47], v56, s[22:23]
	s_cmp_gt_u32 s27, 6
	s_cbranch_scc1 .Lpb_skip
	s_cmp_eq_u32 s27, 6
	s_cbranch_scc1 .Lpb_fc
	s_mov_b64 s[8:9], s[40:41]
	s_mov_b64 s[22:23], s[42:43]
	s_mov_b32 s4, s27
	s_cmp_lt_u32 s27, 3
	s_cbranch_scc1 .Lpb_l1
	s_mov_b64 s[8:9], s[46:47]
	s_mov_b64 s[22:23], s[48:49]
	s_sub_u32 s4, s27, 3

.Lpr2_nowrite:
	s_movk_i32 s4, 0x1a0
	v_add_u32_e32 v59, s29, v69
	v_cmp_gt_u32_e32 vcc, s4, v59
	v_add_f32_e32 v50, v78, v79
	v_lshlrev_b32_e32 v18, 2, v59
	s_and_saveexec_b64 s[0:1], vcc
	v_fma_f32 v50, v76, v50, -v77
	ds_write_b32 v18, v50 offset:41984
	s_or_b64 exec, exec, s[0:1]
	s_mov_b64 s[14:15], s[58:59]
	s_waitcnt lgkmcnt(0)
	v_mov_b32_e32 v18, 0xbfb8aa3b
	s_lshl_b32 s3, s21, 4
	s_cmpk_gt_i32 s20, 0x7fff
	v_cmp_gt_u32_e32 vcc, 32, v69
	s_waitcnt lgkmcnt(0)
	v_mul_f32_e32 v18, s34, v18
	v_exp_f32_e32 v70, v18
	v_mov_b32_e32 v18, 0
	v_and_b32_e32 v71, 48, v0
	s_mov_b32 s10, s20
	s_barrier
	s_cbranch_scc1 .LBB0_37
	s_sub_i32 s2, s20, s3
	s_add_i32 s9, s3, s20
	s_mov_b32 s4, 1.0
	s_mov_b32 s8, 0x3fb4c4be
	v_lshlrev_b32_e32 v72, 4, v69
	v_cmp_eq_u32_e64 s[0:1], 1, v1
	v_lshl_add_u32 v38, s2, 5, v69
	s_lshl_b32 s7, s21, 9
	v_mov_b32_e32 v18, 0
	s_mov_b32 s12, 0
	s_mov_b32 s2, 0x4a000000
	s_mov_b32 s5, s4
	s_mov_b32 s6, 0x3f34c4be
	v_mov_b64_e32 v[40:41], s[8:9]
	s_mov_b32 s8, 0x400a34e2
	s_mov_b32 s33, 0
	s_branch .LBB0_35
.LBB0_34:
	s_or_b64 exec, exec, s[10:11]
	ds_read_b128 v[18:21], v72
	s_waitcnt vmcnt(2)
	v_cvt_pk_f16_f32 v14, v14, v15
	v_cvt_pk_f16_f32 v15, v16, v17
	v_cvt_pk_f16_f32 v16, v10, v11
	ds_read_b128 v[22:25], v71 offset:41984
	v_cvt_pk_f16_f32 v17, v12, v13
	ds_read_b128 v[10:13], v72 offset:1024
	ds_read_b128 v[26:29], v71 offset:42048
	s_waitcnt vmcnt(0)
	v_cvt_pk_f16_f32 v0, v6, v7
	v_cvt_pk_f16_f32 v1, v8, v9
	v_cvt_pk_f16_f32 v2, v2, v3
	v_cvt_pk_f16_f32 v3, v4, v5
	s_waitcnt lgkmcnt(2)
	v_mfma_f32_16x16x32_f16 v[30:33], v[18:21], v[14:17], v[22:25]
	s_add_i32 s10, s20, s12
	v_mfma_f32_16x16x32_f16 v[18:21], v[18:21], v[0:3], v[22:25]
	ds_read_b128 v[4:7], v72 offset:2048
	s_nop 1
	ds_read_b128 v[22:25], v71 offset:42112
	s_waitcnt lgkmcnt(2)
	v_mfma_f32_16x16x32_f16 v[34:37], v[10:13], v[14:17], v[26:29]
	v_exp_f32_e32 v78, v30
	v_exp_f32_e32 v79, v31
	v_exp_f32_e32 v20, v20
	v_mfma_f32_16x16x32_f16 v[8:11], v[10:13], v[0:3], v[26:29]
	ds_read_b128 v[44:47], v71 offset:42176
	s_nop 2
	v_exp_f32_e64 v80, v34 clamp
	v_exp_f32_e64 v81, v35 clamp
	ds_read_b128 v[26:29], v72 offset:3072
	s_waitcnt lgkmcnt(2)
	v_mfma_f32_16x16x32_f16 v[48:51], v[4:7], v[14:17], v[22:25]
	v_exp_f32_e64 v82, v36 clamp
	v_exp_f32_e64 v83, v37 clamp
	v_exp_f32_e32 v21, v21
	v_mfma_f32_16x16x32_f16 v[22:25], v[4:7], v[0:3], v[22:25]
	ds_read_b128 v[52:55], v72 offset:4096
	ds_read_b128 v[56:59], v71 offset:42240
	s_nop 1
	v_exp_f32_e32 v4, v48
	s_waitcnt lgkmcnt(2)
	v_mfma_f32_16x16x32_f16 v[60:63], v[26:29], v[14:17], v[44:47]
	v_exp_f32_e32 v5, v49
	v_exp_f32_e32 v48, v32
	v_exp_f32_e32 v49, v33
	v_mfma_f32_16x16x32_f16 v[26:29], v[26:29], v[0:3], v[44:47]
	ds_read_b128 v[64:67], v71 offset:42304
	v_exp_f32_e32 v6, v50
	v_exp_f32_e32 v7, v51
	ds_read_b128 v[44:47], v72 offset:5120
	s_waitcnt lgkmcnt(2)
	v_mfma_f32_16x16x32_f16 v[74:77], v[52:55], v[14:17], v[56:59]
	v_exp_f32_e32 v50, v18
	v_exp_f32_e32 v51, v19
	v_exp_f32_e32 v26, v26
	v_mfma_f32_16x16x32_f16 v[30:33], v[52:55], v[0:3], v[56:59]
	v_exp_f32_e64 v52, v8 clamp
	v_exp_f32_e64 v53, v9 clamp
	v_exp_f32_e32 v8, v22
	s_waitcnt lgkmcnt(0)
	v_mfma_f32_16x16x32_f16 v[34:37], v[44:47], v[14:17], v[64:67]
	v_exp_f32_e32 v9, v23
	v_exp_f32_e64 v22, v10 clamp
	v_exp_f32_e64 v23, v11 clamp
	v_mfma_f32_16x16x32_f16 v[44:47], v[44:47], v[0:3], v[64:67]
	v_exp_f32_e32 v10, v24
	v_exp_f32_e32 v11, v25
	s_nop 1
	v_exp_f32_e32 v12, v34
	v_exp_f32_e32 v13, v35
	v_exp_f32_e32 v18, v36
	v_exp_f32_e32 v24, v60
	v_exp_f32_e32 v25, v61
	v_exp_f32_e64 v54, v74 clamp
	v_exp_f32_e64 v55, v75 clamp
	v_exp_f32_e32 v34, v62
	v_exp_f32_e32 v35, v63
	v_exp_f32_e64 v56, v76 clamp
	v_exp_f32_e64 v57, v77 clamp
	v_exp_f32_e32 v19, v37
	v_exp_f32_e32 v27, v27
	v_exp_f32_e64 v30, v30 clamp
	v_exp_f32_e64 v31, v31 clamp
	v_exp_f32_e32 v36, v44
	v_exp_f32_e32 v37, v45
	v_exp_f32_e32 v28, v28
	v_exp_f32_e32 v29, v29
	v_exp_f32_e64 v32, v32 clamp
	v_exp_f32_e64 v33, v33 clamp
	v_exp_f32_e32 v44, v46
	v_exp_f32_e32 v45, v47
	v_pk_fma_f32 v[58:59], v[80:81], s[2:3], 1.0 op_sel_hi:[1,0,0]
	v_pk_fma_f32 v[60:61], v[82:83], s[2:3], 1.0 op_sel_hi:[1,0,0]
	v_pk_fma_f32 v[52:53], v[52:53], s[2:3], 1.0 op_sel_hi:[1,0,0]
	v_pk_fma_f32 v[22:23], v[22:23], s[2:3], 1.0 op_sel_hi:[1,0,0]
	v_pk_fma_f32 v[54:55], v[54:55], s[2:3], 1.0 op_sel_hi:[1,0,0]
	v_pk_fma_f32 v[56:57], v[56:57], s[2:3], 1.0 op_sel_hi:[1,0,0]
	v_pk_fma_f32 v[30:31], v[30:31], s[2:3], 1.0 op_sel_hi:[1,0,0]
	v_pk_fma_f32 v[32:33], v[32:33], s[2:3], 1.0 op_sel_hi:[1,0,0]
	v_pk_fma_f32 v[46:47], v[78:79], v[58:59], v[58:59]
	v_pk_fma_f32 v[48:49], v[48:49], v[60:61], v[60:61]
	v_pk_fma_f32 v[50:51], v[50:51], v[52:53], v[52:53]
	v_pk_fma_f32 v[20:21], v[20:21], v[22:23], v[22:23]
	v_pk_fma_f32 v[24:25], v[24:25], v[54:55], v[54:55]
	v_pk_fma_f32 v[34:35], v[34:35], v[56:57], v[56:57]
	v_pk_fma_f32 v[26:27], v[26:27], v[30:31], v[30:31]
	v_pk_fma_f32 v[28:29], v[28:29], v[32:33], v[32:33]
	v_pk_fma_f32 v[58:59], v[58:59], s[6:7], v[40:41] op_sel_hi:[1,0,0] neg_lo:[1,0,0] neg_hi:[1,0,0]
	v_pk_fma_f32 v[60:61], v[60:61], s[6:7], v[40:41] op_sel_hi:[1,0,0] neg_lo:[1,0,0] neg_hi:[1,0,0]
	v_pk_fma_f32 v[52:53], v[52:53], s[6:7], v[40:41] op_sel_hi:[1,0,0] neg_lo:[1,0,0] neg_hi:[1,0,0]
	v_pk_fma_f32 v[22:23], v[22:23], s[6:7], v[40:41] op_sel_hi:[1,0,0] neg_lo:[1,0,0] neg_hi:[1,0,0]
	v_pk_fma_f32 v[54:55], v[54:55], s[6:7], v[40:41] op_sel_hi:[1,0,0] neg_lo:[1,0,0] neg_hi:[1,0,0]
	v_pk_fma_f32 v[56:57], v[56:57], s[6:7], v[40:41] op_sel_hi:[1,0,0] neg_lo:[1,0,0] neg_hi:[1,0,0]
	v_pk_fma_f32 v[30:31], v[30:31], s[6:7], v[40:41] op_sel_hi:[1,0,0] neg_lo:[1,0,0] neg_hi:[1,0,0]
	v_pk_fma_f32 v[32:33], v[32:33], s[6:7], v[40:41] op_sel_hi:[1,0,0] neg_lo:[1,0,0] neg_hi:[1,0,0]
	v_pk_fma_f32 v[46:47], v[4:5], v[46:47], v[46:47]
	v_pk_fma_f32 v[48:49], v[6:7], v[48:49], v[48:49]
	v_pk_fma_f32 v[50:51], v[8:9], v[50:51], v[50:51]
	v_pk_fma_f32 v[20:21], v[10:11], v[20:21], v[20:21]
	v_pk_fma_f32 v[24:25], v[12:13], v[24:25], v[24:25]
	v_pk_fma_f32 v[34:35], v[18:19], v[34:35], v[34:35]
	v_pk_fma_f32 v[26:27], v[36:37], v[26:27], v[26:27]
	v_pk_fma_f32 v[28:29], v[44:45], v[28:29], v[28:29]
	v_rcp_f32_e64 v46, v46 clamp
	v_rcp_f32_e64 v47, v47 clamp
	v_rcp_f32_e64 v48, v48 clamp
	v_rcp_f32_e64 v49, v49 clamp
	v_rcp_f32_e64 v50, v50 clamp
	v_rcp_f32_e64 v51, v51 clamp
	v_rcp_f32_e64 v20, v20 clamp
	v_rcp_f32_e64 v21, v21 clamp
	v_rcp_f32_e64 v24, v24 clamp
	v_rcp_f32_e64 v25, v25 clamp
	v_rcp_f32_e64 v34, v34 clamp
	v_rcp_f32_e64 v35, v35 clamp
	v_rcp_f32_e64 v26, v26 clamp
	v_rcp_f32_e64 v27, v27 clamp
	v_rcp_f32_e64 v28, v28 clamp
	v_rcp_f32_e64 v29, v29 clamp
	v_pk_mul_f32 v[46:47], v[58:59], v[46:47]
	v_pk_mul_f32 v[48:49], v[60:61], v[48:49]
	v_pk_mul_f32 v[50:51], v[52:53], v[50:51]
	v_pk_mul_f32 v[20:21], v[22:23], v[20:21]
	v_pk_mul_f32 v[22:23], v[54:55], v[24:25]
	v_pk_mul_f32 v[24:25], v[56:57], v[34:35]
	v_pk_mul_f32 v[26:27], v[30:31], v[26:27]
	v_pk_mul_f32 v[28:29], v[32:33], v[28:29]
	v_pk_fma_f32 v[4:5], v[4:5], v[46:47], v[46:47]
	v_pk_fma_f32 v[6:7], v[6:7], v[48:49], v[48:49]
	v_pk_fma_f32 v[8:9], v[8:9], v[50:51], v[50:51]
	v_pk_fma_f32 v[10:11], v[10:11], v[20:21], v[20:21]
	v_pk_fma_f32 v[12:13], v[12:13], v[22:23], v[22:23]
	v_pk_fma_f32 v[18:19], v[18:19], v[24:25], v[24:25]
	v_pk_fma_f32 v[30:31], v[36:37], v[26:27], v[26:27]
	v_pk_fma_f32 v[32:33], v[44:45], v[28:29], v[28:29]
	s_nop 0
	v_pk_fma_f32 v[4:5], v[4:5], v[4:5], s[4:5] neg_lo:[1,0,0] neg_hi:[1,0,0] clamp
	v_pk_fma_f32 v[6:7], v[6:7], v[6:7], s[4:5] neg_lo:[1,0,0] neg_hi:[1,0,0] clamp
	v_pk_fma_f32 v[8:9], v[8:9], v[8:9], s[4:5] neg_lo:[1,0,0] neg_hi:[1,0,0] clamp
	v_pk_fma_f32 v[10:11], v[10:11], v[10:11], s[4:5] neg_lo:[1,0,0] neg_hi:[1,0,0] clamp
	v_pk_fma_f32 v[12:13], v[12:13], v[12:13], s[4:5] neg_lo:[1,0,0] neg_hi:[1,0,0] clamp
	v_pk_fma_f32 v[18:19], v[18:19], v[18:19], s[4:5] neg_lo:[1,0,0] neg_hi:[1,0,0] clamp
	v_pk_fma_f32 v[30:31], v[30:31], v[30:31], s[4:5] neg_lo:[1,0,0] neg_hi:[1,0,0] clamp
	s_nop 0
	v_pk_fma_f32 v[32:33], v[32:33], v[32:33], s[4:5] neg_lo:[1,0,0] neg_hi:[1,0,0] clamp
	s_nop 0
	v_pk_fma_f32 v[8:9], v[8:9], v[8:9], s[8:9] op_sel_hi:[1,1,0]
	v_pk_fma_f32 v[10:11], v[10:11], v[10:11], s[8:9] op_sel_hi:[1,1,0]
	v_pk_fma_f32 v[12:13], v[12:13], v[12:13], s[8:9] op_sel_hi:[1,1,0]
	v_pk_fma_f32 v[18:19], v[18:19], v[18:19], s[8:9] op_sel_hi:[1,1,0]
	v_pk_fma_f32 v[32:33], v[32:33], v[32:33], s[8:9] op_sel_hi:[1,1,0]
	v_pk_fma_f32 v[4:5], v[4:5], v[4:5], s[8:9] op_sel_hi:[1,1,0]
	v_pk_fma_f32 v[6:7], v[6:7], v[6:7], s[8:9] op_sel_hi:[1,1,0]
	v_pk_fma_f32 v[30:31], v[30:31], v[30:31], s[8:9] op_sel_hi:[1,1,0]
	v_pk_mul_f32 v[8:9], v[50:51], v[8:9]
	v_pk_mul_f32 v[84:85], v[20:21], v[10:11]
	v_pk_mul_f32 v[86:87], v[22:23], v[12:13]
	v_pk_mul_f32 v[10:11], v[24:25], v[18:19]
	v_pk_mul_f32 v[12:13], v[28:29], v[32:33]
	v_pk_mul_f32 v[64:65], v[46:47], v[4:5]
	v_pk_mul_f32 v[82:83], v[48:49], v[6:7]
	v_pk_mul_f32 v[20:21], v[30:31], v[26:27]
	ds_read_b128 v[4:7], v72 offset:6144
	ds_read_b128 v[22:25], v71 offset:42368
	ds_read_b128 v[26:29], v72 offset:7168
	ds_read_b128 v[30:33], v71 offset:42432
	v_cvt_pk_f16_f32 v19, v84, v85
	v_cvt_pk_f16_f32 v18, v8, v9
	v_cvt_pk_f16_f32 v20, v20, v21
	v_cvt_pk_f16_f32 v21, v12, v13
	s_waitcnt lgkmcnt(2)
	v_mfma_f32_16x16x32_f16 v[34:37], v[4:7], v[14:17], v[22:25]
	v_mfma_f32_16x16x32_f16 v[44:47], v[4:7], v[0:3], v[22:25]
	ds_read_b128 v[4:7], v72 offset:8192
	ds_read_b128 v[48:51], v71 offset:42496
	s_waitcnt lgkmcnt(2)
	v_mfma_f32_16x16x32_f16 v[52:55], v[26:29], v[14:17], v[30:33]
	v_cvt_pk_f16_f32 v22, v64, v65
	v_cvt_pk_f16_f32 v23, v82, v83
	v_cvt_pk_f16_f32 v24, v86, v87
	v_mfma_f32_16x16x32_f16 v[26:29], v[26:29], v[0:3], v[30:33]
	ds_read_b128 v[56:59], v71 offset:42560
	v_exp_f32_e32 v86, v34
	v_exp_f32_e32 v87, v35
	ds_read_b128 v[30:33], v72 offset:9216
	s_waitcnt lgkmcnt(2)
	v_mfma_f32_16x16x32_f16 v[60:63], v[4:7], v[14:17], v[48:51]
	v_exp_f32_e64 v88, v52 clamp
	v_exp_f32_e64 v89, v53 clamp
	v_exp_f32_e64 v90, v54 clamp
	v_mfma_f32_16x16x32_f16 v[48:51], v[4:7], v[0:3], v[48:51]
	ds_read_b128 v[64:67], v72 offset:10240
	ds_read_b128 v[74:77], v71 offset:42624
	s_nop 1
	v_exp_f32_e32 v4, v60
	s_waitcnt lgkmcnt(2)
	v_mfma_f32_16x16x32_f16 v[78:81], v[30:33], v[14:17], v[56:59]
	v_exp_f32_e32 v5, v61
	v_exp_f32_e32 v60, v36
	v_exp_f32_e32 v61, v37
	v_mfma_f32_16x16x32_f16 v[30:33], v[30:33], v[0:3], v[56:59]
	ds_read_b128 v[82:85], v71 offset:42688
	v_exp_f32_e64 v91, v55 clamp
	v_exp_f32_e32 v6, v62
	ds_read_b128 v[56:59], v72 offset:11264
	s_waitcnt lgkmcnt(2)
	v_mfma_f32_16x16x32_f16 v[34:37], v[64:67], v[14:17], v[74:77]
	v_exp_f32_e32 v7, v63
	v_exp_f32_e32 v8, v48
	v_exp_f32_e32 v9, v49
	v_mfma_f32_16x16x32_f16 v[52:55], v[64:67], v[0:3], v[74:77]
	v_exp_f32_e32 v44, v44
	v_exp_f32_e32 v45, v45
	v_exp_f32_e64 v26, v26 clamp
	s_waitcnt lgkmcnt(0)
	v_mfma_f32_16x16x32_f16 v[14:17], v[56:59], v[14:17], v[82:85]
	v_exp_f32_e64 v27, v27 clamp
	v_exp_f32_e32 v46, v46
	v_exp_f32_e32 v47, v47
	v_mfma_f32_16x16x32_f16 v[56:59], v[56:59], v[0:3], v[82:85]
	v_exp_f32_e64 v28, v28 clamp
	s_nop 2
	v_exp_f32_e32 v2, v14
	v_exp_f32_e32 v3, v15
	v_exp_f32_e32 v14, v16
	v_exp_f32_e32 v15, v17
	v_exp_f32_e32 v16, v30
	v_exp_f32_e32 v17, v31
	v_exp_f32_e64 v29, v29 clamp
	v_exp_f32_e32 v0, v50
	v_exp_f32_e32 v1, v51
	v_exp_f32_e32 v48, v78
	v_exp_f32_e32 v49, v79
	v_exp_f32_e64 v34, v34 clamp
	v_exp_f32_e64 v35, v35 clamp
	v_exp_f32_e32 v50, v80
	v_exp_f32_e32 v51, v81
	v_exp_f32_e64 v36, v36 clamp
	v_exp_f32_e64 v37, v37 clamp
	v_exp_f32_e64 v30, v52 clamp
	v_exp_f32_e64 v31, v53 clamp
	v_exp_f32_e32 v52, v56
	v_exp_f32_e32 v53, v57
	v_exp_f32_e32 v32, v32
	v_exp_f32_e32 v33, v33
	v_exp_f32_e64 v54, v54 clamp
	v_exp_f32_e64 v55, v55 clamp
	v_exp_f32_e32 v56, v58
	v_cvt_pk_f16_f32 v25, v10, v11
	v_exp_f32_e32 v57, v59
	v_pk_fma_f32 v[30:31], v[30:31], s[2:3], 1.0 op_sel_hi:[1,0,0]
	v_pk_fma_f32 v[10:11], v[88:89], s[2:3], 1.0 op_sel_hi:[1,0,0]
	v_pk_fma_f32 v[12:13], v[90:91], s[2:3], 1.0 op_sel_hi:[1,0,0]
	v_pk_fma_f32 v[26:27], v[26:27], s[2:3], 1.0 op_sel_hi:[1,0,0]
	v_pk_fma_f32 v[28:29], v[28:29], s[2:3], 1.0 op_sel_hi:[1,0,0]
	v_pk_fma_f32 v[34:35], v[34:35], s[2:3], 1.0 op_sel_hi:[1,0,0]
	v_pk_fma_f32 v[36:37], v[36:37], s[2:3], 1.0 op_sel_hi:[1,0,0]
	v_pk_fma_f32 v[54:55], v[54:55], s[2:3], 1.0 op_sel_hi:[1,0,0]
	v_pk_fma_f32 v[16:17], v[16:17], v[30:31], v[30:31]
	v_pk_fma_f32 v[58:59], v[86:87], v[10:11], v[10:11]
	v_pk_fma_f32 v[10:11], v[10:11], s[6:7], v[40:41] op_sel_hi:[1,0,0] neg_lo:[1,0,0] neg_hi:[1,0,0]
	v_pk_fma_f32 v[60:61], v[60:61], v[12:13], v[12:13]
	v_pk_fma_f32 v[12:13], v[12:13], s[6:7], v[40:41] op_sel_hi:[1,0,0] neg_lo:[1,0,0] neg_hi:[1,0,0]
	v_pk_fma_f32 v[44:45], v[44:45], v[26:27], v[26:27]
	v_pk_fma_f32 v[46:47], v[46:47], v[28:29], v[28:29]
	v_pk_fma_f32 v[48:49], v[48:49], v[34:35], v[34:35]
	v_pk_fma_f32 v[50:51], v[50:51], v[36:37], v[36:37]
	v_pk_fma_f32 v[32:33], v[32:33], v[54:55], v[54:55]
	v_pk_fma_f32 v[16:17], v[52:53], v[16:17], v[16:17]
	v_pk_fma_f32 v[26:27], v[26:27], s[6:7], v[40:41] op_sel_hi:[1,0,0] neg_lo:[1,0,0] neg_hi:[1,0,0]
	v_pk_fma_f32 v[28:29], v[28:29], s[6:7], v[40:41] op_sel_hi:[1,0,0] neg_lo:[1,0,0] neg_hi:[1,0,0]
	v_pk_fma_f32 v[34:35], v[34:35], s[6:7], v[40:41] op_sel_hi:[1,0,0] neg_lo:[1,0,0] neg_hi:[1,0,0]
	v_pk_fma_f32 v[36:37], v[36:37], s[6:7], v[40:41] op_sel_hi:[1,0,0] neg_lo:[1,0,0] neg_hi:[1,0,0]
	v_pk_fma_f32 v[30:31], v[30:31], s[6:7], v[40:41] op_sel_hi:[1,0,0] neg_lo:[1,0,0] neg_hi:[1,0,0]
	v_pk_fma_f32 v[54:55], v[54:55], s[6:7], v[40:41] op_sel_hi:[1,0,0] neg_lo:[1,0,0] neg_hi:[1,0,0]
	v_pk_fma_f32 v[58:59], v[4:5], v[58:59], v[58:59]
	v_pk_fma_f32 v[60:61], v[6:7], v[60:61], v[60:61]
	v_pk_fma_f32 v[44:45], v[8:9], v[44:45], v[44:45]
	v_pk_fma_f32 v[46:47], v[0:1], v[46:47], v[46:47]
	v_pk_fma_f32 v[48:49], v[2:3], v[48:49], v[48:49]
	v_pk_fma_f32 v[50:51], v[14:15], v[50:51], v[50:51]
	v_pk_fma_f32 v[32:33], v[56:57], v[32:33], v[32:33]
	v_rcp_f32_e64 v16, v16 clamp
	v_rcp_f32_e64 v17, v17 clamp
	v_rcp_f32_e64 v58, v58 clamp
	v_rcp_f32_e64 v59, v59 clamp
	v_rcp_f32_e64 v60, v60 clamp
	v_rcp_f32_e64 v61, v61 clamp
	v_rcp_f32_e64 v44, v44 clamp
	v_rcp_f32_e64 v45, v45 clamp
	v_rcp_f32_e64 v46, v46 clamp
	v_rcp_f32_e64 v47, v47 clamp
	v_rcp_f32_e64 v48, v48 clamp
	v_rcp_f32_e64 v49, v49 clamp
	v_rcp_f32_e64 v50, v50 clamp
	v_rcp_f32_e64 v51, v51 clamp
	v_rcp_f32_e64 v32, v32 clamp
	v_rcp_f32_e64 v33, v33 clamp
	v_pk_mul_f32 v[10:11], v[10:11], v[58:59]
	v_pk_mul_f32 v[12:13], v[12:13], v[60:61]
	v_pk_mul_f32 v[26:27], v[26:27], v[44:45]
	v_pk_mul_f32 v[34:35], v[34:35], v[48:49]
	v_pk_mul_f32 v[36:37], v[36:37], v[50:51]
	v_pk_mul_f32 v[28:29], v[28:29], v[46:47]
	v_pk_mul_f32 v[16:17], v[30:31], v[16:17]
	v_pk_mul_f32 v[30:31], v[54:55], v[32:33]
	v_pk_fma_f32 v[4:5], v[4:5], v[10:11], v[10:11]
	v_pk_fma_f32 v[6:7], v[6:7], v[12:13], v[12:13]
	v_pk_fma_f32 v[8:9], v[8:9], v[26:27], v[26:27]
	v_pk_fma_f32 v[2:3], v[2:3], v[34:35], v[34:35]
	v_pk_fma_f32 v[14:15], v[14:15], v[36:37], v[36:37]
	v_pk_fma_f32 v[0:1], v[0:1], v[28:29], v[28:29]
	v_pk_fma_f32 v[32:33], v[52:53], v[16:17], v[16:17]
	v_pk_fma_f32 v[44:45], v[56:57], v[30:31], v[30:31]
	s_nop 0
	v_pk_fma_f32 v[4:5], v[4:5], v[4:5], s[4:5] neg_lo:[1,0,0] neg_hi:[1,0,0] clamp
	v_pk_fma_f32 v[6:7], v[6:7], v[6:7], s[4:5] neg_lo:[1,0,0] neg_hi:[1,0,0] clamp
	v_pk_fma_f32 v[8:9], v[8:9], v[8:9], s[4:5] neg_lo:[1,0,0] neg_hi:[1,0,0] clamp
	v_pk_fma_f32 v[0:1], v[0:1], v[0:1], s[4:5] neg_lo:[1,0,0] neg_hi:[1,0,0] clamp
	v_pk_fma_f32 v[2:3], v[2:3], v[2:3], s[4:5] neg_lo:[1,0,0] neg_hi:[1,0,0] clamp
	v_pk_fma_f32 v[14:15], v[14:15], v[14:15], s[4:5] neg_lo:[1,0,0] neg_hi:[1,0,0] clamp
	v_pk_fma_f32 v[32:33], v[32:33], v[32:33], s[4:5] neg_lo:[1,0,0] neg_hi:[1,0,0] clamp
	s_nop 0
	v_pk_fma_f32 v[44:45], v[44:45], v[44:45], s[4:5] neg_lo:[1,0,0] neg_hi:[1,0,0] clamp
	s_nop 0
	v_pk_fma_f32 v[32:33], v[32:33], v[32:33], s[8:9] op_sel_hi:[1,1,0]
	v_pk_fma_f32 v[4:5], v[4:5], v[4:5], s[8:9] op_sel_hi:[1,1,0]
	v_pk_fma_f32 v[6:7], v[6:7], v[6:7], s[8:9] op_sel_hi:[1,1,0]
	v_pk_fma_f32 v[8:9], v[8:9], v[8:9], s[8:9] op_sel_hi:[1,1,0]
	v_pk_fma_f32 v[0:1], v[0:1], v[0:1], s[8:9] op_sel_hi:[1,1,0]
	v_pk_fma_f32 v[2:3], v[2:3], v[2:3], s[8:9] op_sel_hi:[1,1,0]
	v_pk_fma_f32 v[14:15], v[14:15], v[14:15], s[8:9] op_sel_hi:[1,1,0]
	v_pk_fma_f32 v[44:45], v[44:45], v[44:45], s[8:9] op_sel_hi:[1,1,0]
	v_pk_mul_f32 v[16:17], v[32:33], v[16:17]
	v_pk_mul_f32 v[52:53], v[10:11], v[4:5]
	v_pk_mul_f32 v[54:55], v[12:13], v[6:7]
	v_pk_mul_f32 v[26:27], v[26:27], v[8:9]
	v_pk_mul_f32 v[28:29], v[28:29], v[0:1]
	v_pk_mul_f32 v[56:57], v[34:35], v[2:3]
	v_pk_mul_f32 v[58:59], v[36:37], v[14:15]
	v_pk_mul_f32 v[60:61], v[30:31], v[44:45]
	ds_read_b128 v[0:3], v72 offset:12288
	ds_read_b128 v[4:7], v71 offset:42752
	ds_read_b128 v[8:11], v72 offset:13312
	ds_read_b128 v[12:15], v72 offset:14336
	ds_read_b128 v[34:37], v72 offset:15360
	ds_read_b128 v[44:47], v71 offset:42816
	v_cvt_pk_f16_f32 v30, v52, v53
	v_cvt_pk_f16_f32 v26, v26, v27
	v_cvt_pk_f16_f32 v31, v54, v55
	s_waitcnt lgkmcnt(4)
	v_mfma_f32_16x16x32_f16 v[48:51], v[0:3], v[22:25], v[4:7]
	v_cvt_pk_f16_f32 v32, v56, v57
	v_cvt_pk_f16_f32 v33, v58, v59
	v_cvt_pk_f16_f32 v27, v28, v29
	v_mfma_f32_16x16x32_f16 v[0:3], v[0:3], v[18:21], v[4:7]
	v_cvt_pk_f16_f32 v28, v16, v17
	v_cvt_pk_f16_f32 v29, v60, v61
	s_add_i32 s11, s9, s12
	s_waitcnt lgkmcnt(3)
	v_mfma_f32_16x16x32_f16 v[48:51], v[8:11], v[30:33], v[48:51]
	s_cmp_lt_i32 s11, 0x8000
	s_cselect_b32 s10, s11, s10
	s_ashr_i32 s11, s10, 31
	v_mfma_f32_16x16x32_f16 v[52:55], v[8:11], v[26:29], v[0:3]
	ds_read_b128 v[4:7], v72 offset:17408
	ds_read_b128 v[8:11], v71 offset:42880
	s_lshl_b64 s[10:11], s[10:11], 12
	ds_read_b128 v[0:3], v72 offset:16384
	s_waitcnt lgkmcnt(3)
	v_mfma_f32_16x16x32_f16 v[56:59], v[12:15], v[22:25], v[44:47]
	v_exp_f32_e32 v106, v48
	v_exp_f32_e32 v107, v49
	v_exp_f32_e32 v110, v50
	v_mfma_f32_16x16x32_f16 v[12:15], v[12:15], v[18:21], v[44:47]
	v_exp_f32_e32 v111, v51
	v_exp_f32_e32 v114, v52
	v_exp_f32_e32 v115, v53
	v_mfma_f32_16x16x32_f16 v[44:47], v[34:37], v[30:33], v[56:59]
	v_mfma_f32_16x16x32_f16 v[56:59], v[34:37], v[26:29], v[12:15]
	ds_read_b128 v[34:37], v72 offset:19456
	ds_read_b128 v[60:63], v71 offset:42944
	s_nop 4
	v_exp_f32_e64 v108, v44 clamp
	ds_read_b128 v[12:15], v72 offset:18432
	s_waitcnt lgkmcnt(3)
	v_mfma_f32_16x16x32_f16 v[64:67], v[0:3], v[22:25], v[8:11]
	v_exp_f32_e64 v109, v45 clamp
	v_exp_f32_e64 v112, v46 clamp
	v_exp_f32_e64 v113, v47 clamp
	v_mfma_f32_16x16x32_f16 v[0:3], v[0:3], v[18:21], v[8:11]
	v_exp_f32_e64 v116, v56 clamp
	v_exp_f32_e64 v117, v57 clamp
	v_exp_f32_e64 v58, v58 clamp
	v_mfma_f32_16x16x32_f16 v[64:67], v[4:7], v[30:33], v[64:67]
	v_exp_f32_e64 v59, v59 clamp
	v_mfma_f32_16x16x32_f16 v[74:77], v[4:7], v[26:29], v[0:3]
	ds_read_b128 v[78:81], v72 offset:20480
	ds_read_b128 v[82:85], v72 offset:21504
	ds_read_b128 v[86:89], v71 offset:43008
	s_waitcnt lgkmcnt(3)
	v_mfma_f32_16x16x32_f16 v[6:9], v[12:15], v[22:25], v[60:63]
	v_lshl_or_b32 v0, v68, 7, s10
	v_mov_b32_e32 v1, s11
	v_lshl_add_u64 v[0:1], v[42:43], 0, v[0:1]
	v_mfma_f32_16x16x32_f16 v[60:63], v[12:15], v[18:21], v[60:63]
	global_load_dwordx4 v[10:13], v[0:1], off offset:16
	global_load_dwordx4 v[14:17], v[0:1], off
	global_load_dwordx4 v[2:5], v[0:1], off offset:2064
	v_mfma_f32_16x16x32_f16 v[90:93], v[34:37], v[30:33], v[6:9]
	v_mfma_f32_16x16x32_f16 v[60:63], v[34:37], v[26:29], v[60:63]
	s_nop 1
	global_load_dwordx4 v[6:9], v[0:1], off offset:2048
	ds_read_b128 v[94:97], v72 offset:22528
	ds_read_b128 v[98:101], v72 offset:23552
	ds_read_b128 v[102:105], v71 offset:43072
	s_waitcnt lgkmcnt(3)
	v_mfma_f32_16x16x32_f16 v[44:47], v[78:81], v[22:25], v[86:89]
	v_exp_f32_e32 v0, v64
	v_exp_f32_e32 v1, v65
	v_exp_f32_e32 v34, v66
	v_mfma_f32_16x16x32_f16 v[48:51], v[78:81], v[18:21], v[86:89]
	v_exp_f32_e32 v35, v67
	v_exp_f32_e32 v36, v74
	v_exp_f32_e32 v37, v75
	v_mfma_f32_16x16x32_f16 v[64:67], v[82:85], v[30:33], v[44:47]
	v_exp_f32_e32 v74, v54
	v_exp_f32_e32 v75, v55
	v_exp_f32_e32 v78, v92
	v_mfma_f32_16x16x32_f16 v[50:53], v[82:85], v[26:29], v[48:51]
	v_exp_f32_e32 v44, v76
	v_exp_f32_e32 v45, v77
	v_exp_f32_e32 v76, v90
	s_waitcnt lgkmcnt(0)
	v_mfma_f32_16x16x32_f16 v[46:49], v[94:97], v[22:25], v[102:105]
	v_exp_f32_e32 v77, v91
	v_exp_f32_e64 v64, v64 clamp
	v_exp_f32_e64 v65, v65 clamp
	v_mfma_f32_16x16x32_f16 v[54:57], v[94:97], v[18:21], v[102:105]
	v_exp_f32_e32 v79, v93
	v_exp_f32_e64 v66, v66 clamp
	v_exp_f32_e64 v67, v67 clamp
	v_mfma_f32_16x16x32_f16 v[46:49], v[98:101], v[30:33], v[46:49]
	v_exp_f32_e32 v60, v60
	v_exp_f32_e32 v61, v61
	v_exp_f32_e64 v50, v50 clamp
	v_mfma_f32_16x16x32_f16 v[54:57], v[98:101], v[26:29], v[54:57]
	v_exp_f32_e64 v51, v51 clamp
	s_nop 2
	v_exp_f32_e32 v46, v46
	v_exp_f32_e32 v47, v47
	v_exp_f32_e32 v48, v48
	v_exp_f32_e32 v49, v49
	v_exp_f32_e32 v54, v54
	v_exp_f32_e32 v55, v55
	v_exp_f32_e32 v62, v62
	v_exp_f32_e32 v63, v63
	v_exp_f32_e64 v52, v52 clamp
	v_exp_f32_e64 v53, v53 clamp
	v_exp_f32_e32 v56, v56
	v_exp_f32_e32 v57, v57
	v_pk_fma_f32 v[80:81], v[108:109], s[2:3], 1.0 op_sel_hi:[1,0,0]
	v_pk_fma_f32 v[82:83], v[112:113], s[2:3], 1.0 op_sel_hi:[1,0,0]
	v_pk_fma_f32 v[84:85], v[116:117], s[2:3], 1.0 op_sel_hi:[1,0,0]
	v_pk_fma_f32 v[58:59], v[58:59], s[2:3], 1.0 op_sel_hi:[1,0,0]
	v_pk_fma_f32 v[64:65], v[64:65], s[2:3], 1.0 op_sel_hi:[1,0,0]
	v_pk_fma_f32 v[66:67], v[66:67], s[2:3], 1.0 op_sel_hi:[1,0,0]
	v_pk_fma_f32 v[50:51], v[50:51], s[2:3], 1.0 op_sel_hi:[1,0,0]
	v_pk_fma_f32 v[52:53], v[52:53], s[2:3], 1.0 op_sel_hi:[1,0,0]
	v_pk_fma_f32 v[86:87], v[106:107], v[80:81], v[80:81]
	v_pk_fma_f32 v[88:89], v[110:111], v[82:83], v[82:83]
	v_pk_fma_f32 v[90:91], v[114:115], v[84:85], v[84:85]
	v_pk_fma_f32 v[74:75], v[74:75], v[58:59], v[58:59]
	v_pk_fma_f32 v[76:77], v[76:77], v[64:65], v[64:65]
	v_pk_fma_f32 v[78:79], v[78:79], v[66:67], v[66:67]
	v_pk_fma_f32 v[60:61], v[60:61], v[50:51], v[50:51]
	v_pk_fma_f32 v[62:63], v[62:63], v[52:53], v[52:53]
	v_pk_fma_f32 v[80:81], v[80:81], s[6:7], v[40:41] op_sel_hi:[1,0,0] neg_lo:[1,0,0] neg_hi:[1,0,0]
	v_pk_fma_f32 v[82:83], v[82:83], s[6:7], v[40:41] op_sel_hi:[1,0,0] neg_lo:[1,0,0] neg_hi:[1,0,0]
	v_pk_fma_f32 v[84:85], v[84:85], s[6:7], v[40:41] op_sel_hi:[1,0,0] neg_lo:[1,0,0] neg_hi:[1,0,0]
	v_pk_fma_f32 v[58:59], v[58:59], s[6:7], v[40:41] op_sel_hi:[1,0,0] neg_lo:[1,0,0] neg_hi:[1,0,0]
	v_pk_fma_f32 v[64:65], v[64:65], s[6:7], v[40:41] op_sel_hi:[1,0,0] neg_lo:[1,0,0] neg_hi:[1,0,0]
	v_pk_fma_f32 v[66:67], v[66:67], s[6:7], v[40:41] op_sel_hi:[1,0,0] neg_lo:[1,0,0] neg_hi:[1,0,0]
	v_pk_fma_f32 v[50:51], v[50:51], s[6:7], v[40:41] op_sel_hi:[1,0,0] neg_lo:[1,0,0] neg_hi:[1,0,0]
	v_pk_fma_f32 v[52:53], v[52:53], s[6:7], v[40:41] op_sel_hi:[1,0,0] neg_lo:[1,0,0] neg_hi:[1,0,0]
	v_pk_fma_f32 v[86:87], v[0:1], v[86:87], v[86:87]
	v_pk_fma_f32 v[88:89], v[34:35], v[88:89], v[88:89]
	v_pk_fma_f32 v[90:91], v[36:37], v[90:91], v[90:91]
	v_pk_fma_f32 v[74:75], v[44:45], v[74:75], v[74:75]
	v_pk_fma_f32 v[76:77], v[46:47], v[76:77], v[76:77]
	v_pk_fma_f32 v[78:79], v[48:49], v[78:79], v[78:79]
	v_pk_fma_f32 v[60:61], v[54:55], v[60:61], v[60:61]
	v_pk_fma_f32 v[62:63], v[56:57], v[62:63], v[62:63]
	v_rcp_f32_e64 v86, v86 clamp
	v_rcp_f32_e64 v87, v87 clamp
	v_rcp_f32_e64 v88, v88 clamp
	v_rcp_f32_e64 v89, v89 clamp
	v_rcp_f32_e64 v90, v90 clamp
	v_rcp_f32_e64 v91, v91 clamp
	v_rcp_f32_e64 v74, v74 clamp
	v_rcp_f32_e64 v75, v75 clamp
	v_rcp_f32_e64 v76, v76 clamp
	v_rcp_f32_e64 v77, v77 clamp
	v_rcp_f32_e64 v78, v78 clamp
	v_rcp_f32_e64 v79, v79 clamp
	v_rcp_f32_e64 v60, v60 clamp
	v_rcp_f32_e64 v61, v61 clamp
	v_rcp_f32_e64 v62, v62 clamp
	v_rcp_f32_e64 v63, v63 clamp
	v_pk_mul_f32 v[80:81], v[80:81], v[86:87]
	v_pk_mul_f32 v[82:83], v[82:83], v[88:89]
	v_pk_mul_f32 v[84:85], v[84:85], v[90:91]
	v_pk_mul_f32 v[58:59], v[58:59], v[74:75]
	v_pk_mul_f32 v[64:65], v[64:65], v[76:77]
	v_pk_mul_f32 v[66:67], v[66:67], v[78:79]
	v_pk_mul_f32 v[50:51], v[50:51], v[60:61]
	v_pk_mul_f32 v[60:61], v[52:53], v[62:63]
	v_pk_fma_f32 v[0:1], v[0:1], v[80:81], v[80:81]
	v_pk_fma_f32 v[34:35], v[34:35], v[82:83], v[82:83]
	v_pk_fma_f32 v[36:37], v[36:37], v[84:85], v[84:85]
	v_pk_fma_f32 v[44:45], v[44:45], v[58:59], v[58:59]
	v_pk_fma_f32 v[46:47], v[46:47], v[64:65], v[64:65]
	v_pk_fma_f32 v[48:49], v[48:49], v[66:67], v[66:67]
	v_pk_fma_f32 v[52:53], v[54:55], v[50:51], v[50:51]
	v_pk_fma_f32 v[54:55], v[56:57], v[60:61], v[60:61]
	s_nop 0
	v_pk_fma_f32 v[0:1], v[0:1], v[0:1], s[4:5] neg_lo:[1,0,0] neg_hi:[1,0,0] clamp
	v_pk_fma_f32 v[34:35], v[34:35], v[34:35], s[4:5] neg_lo:[1,0,0] neg_hi:[1,0,0] clamp
	v_pk_fma_f32 v[36:37], v[36:37], v[36:37], s[4:5] neg_lo:[1,0,0] neg_hi:[1,0,0] clamp
	v_pk_fma_f32 v[44:45], v[44:45], v[44:45], s[4:5] neg_lo:[1,0,0] neg_hi:[1,0,0] clamp
	v_pk_fma_f32 v[46:47], v[46:47], v[46:47], s[4:5] neg_lo:[1,0,0] neg_hi:[1,0,0] clamp
	v_pk_fma_f32 v[48:49], v[48:49], v[48:49], s[4:5] neg_lo:[1,0,0] neg_hi:[1,0,0] clamp
	v_pk_fma_f32 v[52:53], v[52:53], v[52:53], s[4:5] neg_lo:[1,0,0] neg_hi:[1,0,0] clamp
	s_nop 0
	v_pk_fma_f32 v[54:55], v[54:55], v[54:55], s[4:5] neg_lo:[1,0,0] neg_hi:[1,0,0] clamp
	s_nop 0
	v_pk_fma_f32 v[0:1], v[0:1], v[0:1], s[8:9] op_sel_hi:[1,1,0]
	v_pk_fma_f32 v[56:57], v[34:35], v[34:35], s[8:9] op_sel_hi:[1,1,0]
	v_pk_fma_f32 v[36:37], v[36:37], v[36:37], s[8:9] op_sel_hi:[1,1,0]
	v_pk_fma_f32 v[44:45], v[44:45], v[44:45], s[8:9] op_sel_hi:[1,1,0]
	v_pk_fma_f32 v[46:47], v[46:47], v[46:47], s[8:9] op_sel_hi:[1,1,0]
	v_pk_fma_f32 v[48:49], v[48:49], v[48:49], s[8:9] op_sel_hi:[1,1,0]
	v_pk_fma_f32 v[62:63], v[52:53], v[52:53], s[8:9] op_sel_hi:[1,1,0]
	v_pk_fma_f32 v[74:75], v[54:55], v[54:55], s[8:9] op_sel_hi:[1,1,0]
	v_pk_mul_f32 v[34:35], v[80:81], v[0:1]
	v_pk_mul_f32 v[56:57], v[82:83], v[56:57]
	v_pk_mul_f32 v[36:37], v[84:85], v[36:37]
	v_pk_mul_f32 v[52:53], v[58:59], v[44:45]
	v_pk_mul_f32 v[54:55], v[64:65], v[46:47]
	v_pk_mul_f32 v[0:1], v[66:67], v[48:49]
	v_pk_mul_f32 v[46:47], v[62:63], v[50:51]
	v_pk_mul_f32 v[44:45], v[60:61], v[74:75]
	ds_read_b128 v[48:51], v72 offset:24576
	ds_read_b128 v[58:61], v71 offset:43136
	ds_read_b128 v[62:65], v72 offset:25600
	ds_read_b128 v[74:77], v72 offset:26624
	ds_read_b128 v[78:81], v72 offset:27648
	ds_read_b128 v[82:85], v71 offset:43200
	v_cvt_pk_f16_f32 v34, v34, v35
	v_cvt_pk_f16_f32 v35, v56, v57
	s_waitcnt lgkmcnt(4)
	v_mfma_f32_16x16x32_f16 v[86:89], v[48:51], v[22:25], v[58:61]
	v_mfma_f32_16x16x32_f16 v[48:51], v[48:51], v[18:21], v[58:61]
	s_waitcnt lgkmcnt(3)
	v_mfma_f32_16x16x32_f16 v[58:61], v[62:65], v[30:33], v[86:89]
	v_mfma_f32_16x16x32_f16 v[86:89], v[62:65], v[26:29], v[48:51]
	ds_read_b128 v[62:65], v72 offset:29696
	ds_read_b128 v[90:93], v71 offset:43264
	s_nop 2
	ds_read_b128 v[48:51], v72 offset:28672
	s_waitcnt lgkmcnt(3)
	v_mfma_f32_16x16x32_f16 v[94:97], v[74:77], v[22:25], v[82:85]
	v_exp_f32_e32 v120, v86
	v_exp_f32_e32 v121, v87
	v_exp_f32_e32 v122, v88
	v_mfma_f32_16x16x32_f16 v[74:77], v[74:77], v[18:21], v[82:85]
	v_exp_f32_e32 v123, v89
	v_mfma_f32_16x16x32_f16 v[82:85], v[78:81], v[30:33], v[94:97]
	v_mfma_f32_16x16x32_f16 v[74:77], v[78:81], v[26:29], v[74:77]
	ds_read_b128 v[78:81], v72 offset:30720
	s_nop 0
	ds_read_b128 v[94:97], v72 offset:31744
	ds_read_b128 v[98:101], v71 offset:43328
	s_waitcnt lgkmcnt(3)
	v_mfma_f32_16x16x32_f16 v[102:105], v[48:51], v[22:25], v[90:93]
	s_nop 0
	v_exp_f32_e64 v66, v82 clamp
	v_exp_f32_e64 v67, v83 clamp
	v_exp_f32_e64 v118, v84 clamp
	v_mfma_f32_16x16x32_f16 v[48:51], v[48:51], v[18:21], v[90:93]
	v_exp_f32_e64 v119, v85 clamp
	v_exp_f32_e64 v124, v74 clamp
	v_exp_f32_e64 v125, v75 clamp
	v_mfma_f32_16x16x32_f16 v[90:93], v[62:65], v[30:33], v[102:105]
	v_exp_f32_e64 v126, v76 clamp
	v_exp_f32_e64 v127, v77 clamp
	v_mfma_f32_16x16x32_f16 v[102:105], v[62:65], v[26:29], v[48:51]
	ds_read_b128 v[106:109], v72 offset:32768
	ds_read_b128 v[110:113], v72 offset:33792
	v_exp_f32_e32 v62, v58
	v_exp_f32_e32 v63, v59
	v_exp_f32_e32 v64, v60
	v_exp_f32_e32 v65, v61
	ds_read_b128 v[114:117], v71 offset:43392
	s_waitcnt lgkmcnt(3)
	v_mfma_f32_16x16x32_f16 v[58:61], v[78:81], v[22:25], v[98:101]
	v_exp_f32_e32 v48, v90
	v_exp_f32_e32 v49, v91
	v_exp_f32_e32 v50, v92
	v_mfma_f32_16x16x32_f16 v[78:81], v[78:81], v[18:21], v[98:101]
	v_exp_f32_e32 v51, v93
	v_mfma_f32_16x16x32_f16 v[82:85], v[94:97], v[30:33], v[58:61]
	v_mfma_f32_16x16x32_f16 v[78:81], v[94:97], v[26:29], v[78:81]
	ds_read_b128 v[86:89], v72 offset:34816
	ds_read_b128 v[90:93], v72 offset:35840
	ds_read_b128 v[94:97], v71 offset:43456
	s_waitcnt lgkmcnt(3)
	v_mfma_f32_16x16x32_f16 v[74:77], v[106:109], v[22:25], v[114:117]
	v_exp_f32_e32 v58, v102
	v_exp_f32_e32 v59, v103
	v_exp_f32_e32 v60, v104
	v_mfma_f32_16x16x32_f16 v[98:101], v[106:109], v[18:21], v[114:117]
	v_exp_f32_e32 v61, v105
	v_exp_f32_e32 v102, v82
	v_exp_f32_e32 v103, v83
	v_exp_f32_e32 v104, v84
	v_exp_f32_e32 v105, v85
	v_mfma_f32_16x16x32_f16 v[74:77], v[110:113], v[30:33], v[74:77]
	v_mfma_f32_16x16x32_f16 v[82:85], v[110:113], v[26:29], v[98:101]
	s_waitcnt lgkmcnt(0)
	v_mfma_f32_16x16x32_f16 v[18:21], v[86:89], v[18:21], v[94:97]
	s_nop 4
	v_exp_f32_e64 v106, v74 clamp
	v_exp_f32_e64 v107, v75 clamp
	v_exp_f32_e64 v108, v76 clamp
	v_exp_f32_e64 v109, v77 clamp
	v_mfma_f32_16x16x32_f16 v[74:77], v[86:89], v[22:25], v[94:97]
	v_cvt_pk_f16_f32 v22, v36, v37
	v_cvt_pk_f16_f32 v23, v52, v53
	v_cvt_pk_f16_f32 v36, v54, v55
	v_mfma_f32_16x16x32_f16 v[18:21], v[90:93], v[26:29], v[18:21]
	v_exp_f32_e32 v52, v78
	v_exp_f32_e32 v53, v79
	v_exp_f32_e64 v54, v82 clamp
	v_mfma_f32_16x16x32_f16 v[30:33], v[90:93], v[30:33], v[74:77]
	v_exp_f32_e64 v55, v83 clamp
	s_nop 2
	v_exp_f32_e32 v18, v18
	v_exp_f32_e32 v19, v19
	v_exp_f32_e32 v26, v80
	v_exp_f32_e32 v27, v81
	v_exp_f32_e32 v30, v30
	v_exp_f32_e32 v31, v31
	v_exp_f32_e32 v32, v32
	v_exp_f32_e32 v33, v33
	v_exp_f32_e64 v28, v84 clamp
	v_exp_f32_e64 v29, v85 clamp
	v_exp_f32_e32 v20, v20
	v_cvt_pk_f16_f32 v24, v46, v47
	v_cvt_pk_f16_f32 v37, v0, v1
	v_cvt_pk_f16_f32 v25, v44, v45
	v_exp_f32_e32 v21, v21
	v_pk_fma_f32 v[0:1], v[66:67], s[2:3], 1.0 op_sel_hi:[1,0,0]
	v_pk_fma_f32 v[44:45], v[118:119], s[2:3], 1.0 op_sel_hi:[1,0,0]
	v_pk_fma_f32 v[46:47], v[124:125], s[2:3], 1.0 op_sel_hi:[1,0,0]
	v_pk_fma_f32 v[56:57], v[126:127], s[2:3], 1.0 op_sel_hi:[1,0,0]
	v_pk_fma_f32 v[66:67], v[106:107], s[2:3], 1.0 op_sel_hi:[1,0,0]
	v_pk_fma_f32 v[74:75], v[108:109], s[2:3], 1.0 op_sel_hi:[1,0,0]
	v_pk_fma_f32 v[54:55], v[54:55], s[2:3], 1.0 op_sel_hi:[1,0,0]
	v_pk_fma_f32 v[28:29], v[28:29], s[2:3], 1.0 op_sel_hi:[1,0,0]
	v_pk_fma_f32 v[62:63], v[62:63], v[0:1], v[0:1]
	v_pk_fma_f32 v[64:65], v[64:65], v[44:45], v[44:45]
	v_pk_fma_f32 v[76:77], v[120:121], v[46:47], v[46:47]
	v_pk_fma_f32 v[78:79], v[122:123], v[56:57], v[56:57]
	v_pk_fma_f32 v[80:81], v[102:103], v[66:67], v[66:67]
	v_pk_fma_f32 v[82:83], v[104:105], v[74:75], v[74:75]
	v_pk_fma_f32 v[52:53], v[52:53], v[54:55], v[54:55]
	v_pk_fma_f32 v[26:27], v[26:27], v[28:29], v[28:29]
	v_pk_fma_f32 v[0:1], v[0:1], s[6:7], v[40:41] op_sel_hi:[1,0,0] neg_lo:[1,0,0] neg_hi:[1,0,0]
	v_pk_fma_f32 v[44:45], v[44:45], s[6:7], v[40:41] op_sel_hi:[1,0,0] neg_lo:[1,0,0] neg_hi:[1,0,0]
	v_pk_fma_f32 v[46:47], v[46:47], s[6:7], v[40:41] op_sel_hi:[1,0,0] neg_lo:[1,0,0] neg_hi:[1,0,0]
	v_pk_fma_f32 v[56:57], v[56:57], s[6:7], v[40:41] op_sel_hi:[1,0,0] neg_lo:[1,0,0] neg_hi:[1,0,0]
	v_pk_fma_f32 v[66:67], v[66:67], s[6:7], v[40:41] op_sel_hi:[1,0,0] neg_lo:[1,0,0] neg_hi:[1,0,0]
	v_pk_fma_f32 v[74:75], v[74:75], s[6:7], v[40:41] op_sel_hi:[1,0,0] neg_lo:[1,0,0] neg_hi:[1,0,0]
	v_pk_fma_f32 v[54:55], v[54:55], s[6:7], v[40:41] op_sel_hi:[1,0,0] neg_lo:[1,0,0] neg_hi:[1,0,0]
	v_pk_fma_f32 v[28:29], v[28:29], s[6:7], v[40:41] op_sel_hi:[1,0,0] neg_lo:[1,0,0] neg_hi:[1,0,0]
	v_pk_fma_f32 v[62:63], v[48:49], v[62:63], v[62:63]
	v_pk_fma_f32 v[64:65], v[50:51], v[64:65], v[64:65]
	v_pk_fma_f32 v[76:77], v[58:59], v[76:77], v[76:77]
	v_pk_fma_f32 v[78:79], v[60:61], v[78:79], v[78:79]
	v_pk_fma_f32 v[80:81], v[30:31], v[80:81], v[80:81]
	v_pk_fma_f32 v[82:83], v[32:33], v[82:83], v[82:83]
	v_pk_fma_f32 v[52:53], v[18:19], v[52:53], v[52:53]
	v_pk_fma_f32 v[26:27], v[20:21], v[26:27], v[26:27]
	v_rcp_f32_e64 v62, v62 clamp
	v_rcp_f32_e64 v63, v63 clamp
	v_rcp_f32_e64 v64, v64 clamp
	v_rcp_f32_e64 v65, v65 clamp
	v_rcp_f32_e64 v76, v76 clamp
	v_rcp_f32_e64 v77, v77 clamp
	v_rcp_f32_e64 v78, v78 clamp
	v_rcp_f32_e64 v79, v79 clamp
	v_rcp_f32_e64 v80, v80 clamp
	v_rcp_f32_e64 v81, v81 clamp
	v_rcp_f32_e64 v82, v82 clamp
	v_rcp_f32_e64 v83, v83 clamp
	v_rcp_f32_e64 v52, v52 clamp
	v_rcp_f32_e64 v53, v53 clamp
	v_rcp_f32_e64 v26, v26 clamp
	v_rcp_f32_e64 v27, v27 clamp
	v_pk_mul_f32 v[52:53], v[54:55], v[52:53]
	v_pk_mul_f32 v[0:1], v[0:1], v[62:63]
	v_pk_mul_f32 v[44:45], v[44:45], v[64:65]
	v_pk_mul_f32 v[46:47], v[46:47], v[76:77]
	v_pk_mul_f32 v[56:57], v[56:57], v[78:79]
	v_pk_mul_f32 v[62:63], v[66:67], v[80:81]
	v_pk_mul_f32 v[64:65], v[74:75], v[82:83]
	v_pk_mul_f32 v[26:27], v[28:29], v[26:27]
	v_pk_fma_f32 v[18:19], v[18:19], v[52:53], v[52:53]
	v_pk_fma_f32 v[28:29], v[48:49], v[0:1], v[0:1]
	v_pk_fma_f32 v[48:49], v[50:51], v[44:45], v[44:45]
	v_pk_fma_f32 v[50:51], v[58:59], v[46:47], v[46:47]
	v_pk_fma_f32 v[54:55], v[60:61], v[56:57], v[56:57]
	v_pk_fma_f32 v[30:31], v[30:31], v[62:63], v[62:63]
	v_pk_fma_f32 v[32:33], v[32:33], v[64:65], v[64:65]
	v_pk_fma_f32 v[20:21], v[20:21], v[26:27], v[26:27]
	s_nop 0
	v_pk_fma_f32 v[28:29], v[28:29], v[28:29], s[4:5] neg_lo:[1,0,0] neg_hi:[1,0,0] clamp
	v_pk_fma_f32 v[48:49], v[48:49], v[48:49], s[4:5] neg_lo:[1,0,0] neg_hi:[1,0,0] clamp
	v_pk_fma_f32 v[50:51], v[50:51], v[50:51], s[4:5] neg_lo:[1,0,0] neg_hi:[1,0,0] clamp
	v_pk_fma_f32 v[54:55], v[54:55], v[54:55], s[4:5] neg_lo:[1,0,0] neg_hi:[1,0,0] clamp
	v_pk_fma_f32 v[30:31], v[30:31], v[30:31], s[4:5] neg_lo:[1,0,0] neg_hi:[1,0,0] clamp
	v_pk_fma_f32 v[32:33], v[32:33], v[32:33], s[4:5] neg_lo:[1,0,0] neg_hi:[1,0,0] clamp
	v_pk_fma_f32 v[18:19], v[18:19], v[18:19], s[4:5] neg_lo:[1,0,0] neg_hi:[1,0,0] clamp
	s_nop 0
	v_pk_fma_f32 v[20:21], v[20:21], v[20:21], s[4:5] neg_lo:[1,0,0] neg_hi:[1,0,0] clamp
	s_nop 0
	v_pk_fma_f32 v[28:29], v[28:29], v[28:29], s[8:9] op_sel_hi:[1,1,0]
	v_pk_fma_f32 v[48:49], v[48:49], v[48:49], s[8:9] op_sel_hi:[1,1,0]
	v_pk_fma_f32 v[50:51], v[50:51], v[50:51], s[8:9] op_sel_hi:[1,1,0]
	v_pk_fma_f32 v[54:55], v[54:55], v[54:55], s[8:9] op_sel_hi:[1,1,0]
	v_pk_fma_f32 v[30:31], v[30:31], v[30:31], s[8:9] op_sel_hi:[1,1,0]
	v_pk_fma_f32 v[32:33], v[32:33], v[32:33], s[8:9] op_sel_hi:[1,1,0]
	v_pk_fma_f32 v[18:19], v[18:19], v[18:19], s[8:9] op_sel_hi:[1,1,0]
	v_pk_fma_f32 v[20:21], v[20:21], v[20:21], s[8:9] op_sel_hi:[1,1,0]
	v_pk_mul_f32 v[0:1], v[0:1], v[28:29]
	v_pk_mul_f32 v[58:59], v[44:45], v[48:49]
	v_pk_mul_f32 v[60:61], v[46:47], v[50:51]
	v_pk_mul_f32 v[54:55], v[56:57], v[54:55]
	v_pk_mul_f32 v[62:63], v[62:63], v[30:31]
	v_pk_mul_f32 v[64:65], v[64:65], v[32:33]
	v_pk_mul_f32 v[66:67], v[18:19], v[52:53]
	v_pk_mul_f32 v[74:75], v[26:27], v[20:21]
	ds_read_b128 v[18:21], v72 offset:36864
	ds_read_b128 v[30:33], v72 offset:37888
	ds_read_b128 v[26:29], v71 offset:43520
	v_cvt_pk_f16_f32 v56, v60, v61
	v_cvt_pk_f16_f32 v57, v54, v55
	v_cvt_pk_f16_f32 v54, v62, v63
	ds_read_b128 v[60:63], v71 offset:43584
	v_cvt_pk_f16_f32 v52, v0, v1
	v_cvt_pk_f16_f32 v53, v58, v59
	s_waitcnt lgkmcnt(1)
	v_mfma_f32_16x16x32_f16 v[48:51], v[18:21], v[34:37], v[26:29]
	v_cvt_pk_f16_f32 v55, v64, v65
	v_cvt_pk_f16_f32 v58, v66, v67
	v_cvt_pk_f16_f32 v59, v74, v75
	v_mfma_f32_16x16x32_f16 v[18:21], v[18:21], v[22:25], v[26:29]
	ds_read_b128 v[44:47], v72 offset:40960
	s_add_i32 s12, s12, s3
	s_add_i32 s10, s20, s12
	v_mfma_f32_16x16x32_f16 v[26:29], v[30:33], v[52:55], v[48:51]
	s_cmp_lt_i32 s10, 0x8000
	v_add_u32_e32 v38, s7, v38
	s_nop 0
	ds_read_b128 v[48:51], v72 offset:38912
	v_mfma_f32_16x16x32_f16 v[18:21], v[30:33], v[56:59], v[18:21]
	ds_read_b128 v[30:33], v72 offset:39936
	s_nop 1
	v_cvt_pk_f16_f32 v1, v28, v29
	v_cvt_pk_f16_f32 v0, v26, v27
	s_waitcnt lgkmcnt(1)
	v_mfma_f32_16x16x32_f16 v[34:37], v[48:51], v[34:37], v[60:63]
	v_pk_max_f16 v27, v1, 0
	v_cvt_pk_f16_f32 v1, v20, v21
	v_pk_max_f16 v26, v0, 0
	v_mfma_f32_16x16x32_f16 v[20:23], v[48:51], v[22:25], v[60:63]
	v_cvt_pk_f16_f32 v0, v18, v19
	v_pk_max_f16 v18, v0, 0
	v_pk_max_f16 v19, v1, 0
	s_waitcnt lgkmcnt(0)
	v_mfma_f32_16x16x32_f16 v[34:37], v[30:33], v[52:55], v[34:37]
	v_mfma_f32_16x16x32_f16 v[20:23], v[30:33], v[56:59], v[20:23]
	s_nop 6
	v_cvt_pk_f16_f32 v0, v34, v35
	v_cvt_pk_f16_f32 v1, v36, v37
	v_pk_max_f16 v28, v0, 0
	v_pk_max_f16 v29, v1, 0
	v_cvt_pk_f16_f32 v0, v20, v21
	v_cvt_pk_f16_f32 v1, v22, v23
	v_pk_max_f16 v20, v0, 0
	v_pk_max_f16 v21, v1, 0
	v_mfma_f32_16x16x32_f16 v[24:27], v[44:47], v[26:29], 0
	s_nop 0
	v_mfma_f32_16x16x32_f16 v[18:21], v[44:47], v[18:21], 0
	s_nop 7
	v_cndmask_b32_e64 v18, v24, v18, s[0:1]
	s_cbranch_scc0 .LBB0_37
